# norm2 phase prologue restructured: scalar/param loads, first x rows, g_norm2 and first sample's shift/scale vectors are issued before the LDS router-weight fill and its barrier (latency overlap); per/
# speedup vs baseline: 1.0154x; 1.0047x over previous
.LBB0_1047:
	s_or_b64 exec, exec, s[0:1]
	s_mov_b64 s[12:13], s[72:73]
	v_mov_b32_e32 v18, v0
	s_waitcnt lgkmcnt(0)
	s_barrier
	s_nop 0
	s_mov_b64 s[14:15], exec
	s_mov_b64 s[94:95], 0x40000
	s_load_dwordx2 s[4:5], s[12:13], 0x178
	s_load_dwordx2 s[6:7], s[12:13], 0x130
	s_load_dwordx2 s[8:9], s[12:13], 0x228
	s_load_dwordx2 s[10:11], s[12:13], 0x120
	s_load_dwordx2 s[32:33], s[12:13], 0x38
	s_load_dwordx2 s[34:35], s[12:13], 0xf0
	s_load_dwordx2 s[0:1], s[12:13], 0xe8
	v_readlane_b32 s20, v255, 12
	v_readlane_b32 s36, v255, 6
	v_readlane_b32 s37, v255, 7
	v_and_b32_e32 v229, 63, v18
	v_lshlrev_b32_e32 v230, 3, v229
	v_lshlrev_b32_e32 v231, 4, v229
	v_bfe_u32 v232, v18, 2, 4
	v_lshlrev_b32_e32 v232, 2, v232
	v_and_b32_e32 v233, 8, v18
	v_cmp_eq_u32_e64 s[26:27], 0, v233
	v_and_b32_e32 v233, 4, v18
	v_cmp_eq_u32_e64 s[28:29], 0, v233
	v_and_b32_e32 v233, 3, v18
	v_cmp_eq_u32_e64 s[30:31], 0, v233
	v_mov_b32_e32 v234, 0x358637bd
	v_lshlrev_b32_e32 v220, 4, v18
	v_and_b32_e32 v221, 15, v18
	v_lshrrev_b32_e32 v222, 4, v18
	v_lshlrev_b32_e32 v221, 10, v221
	v_lshl_or_b32 v221, v222, 4, v221
	v_lshrrev_b32_e32 v222, 6, v18
	s_nop 0
	v_readfirstlane_b32 s18, v222
	s_lshl_b32 s19, s2, 3
	s_add_i32 s18, s18, s19
	s_add_i32 s19, s24, 0x7ff
	s_lshr_b32 s19, s19, 11
	s_mul_i32 s18, s18, s19
	s_add_i32 s19, s18, s19
	s_min_i32 s19, s19, s24
	s_mov_b32 s25, 0xffff0000
	s_mul_i32 s16, s20, 9
	s_mov_b32 s17, 0
	s_movk_i32 s22, 0x6000
	s_mul_i32 s21, s16, s22
	s_waitcnt lgkmcnt(0)
	s_add_u32 s0, s0, s36
	s_addc_u32 s1, s1, s37
	global_load_dwordx4 v[116:119], v220, s[0:1]
	s_add_u32 s0, s0, 0x2000
	s_addc_u32 s1, s1, 0
	global_load_dwordx4 v[120:123], v220, s[0:1]
	s_add_u32 s0, s0, 0x2000
	s_addc_u32 s1, s1, 0
	global_load_dwordx4 v[124:127], v220, s[0:1]
	s_add_u32 s0, s0, 0x2000
	s_addc_u32 s1, s1, 0
	global_load_dwordx4 v[128:131], v220, s[0:1]
	s_add_u32 s0, s0, 0x2000
	s_addc_u32 s1, s1, 0
	global_load_dwordx4 v[132:135], v220, s[0:1]
	s_add_u32 s0, s0, 0x2000
	s_addc_u32 s1, s1, 0
	global_load_dwordx4 v[136:139], v220, s[0:1]
	s_add_u32 s0, s0, 0x2000
	s_addc_u32 s1, s1, 0
	global_load_dwordx4 v[140:143], v220, s[0:1]
	s_add_u32 s0, s0, 0x2000
	s_addc_u32 s1, s1, 0
	global_load_dwordx4 v[144:147], v220, s[0:1]
	s_cmp_lt_i32 s18, s19
	s_cbranch_scc0 .Ln2_idle
	s_lshl_b32 s0, s20, 12
	s_lshl_b32 s1, s20, 6
	s_lshl_b32 s23, s18, 11
	s_lshl_b32 s36, s18, 6
	s_add_u32 s10, s10, s21
	s_addc_u32 s11, s11, 0
	s_add_u32 s32, s32, s0
	s_addc_u32 s33, s33, 0
	s_add_u32 s34, s34, s1
	s_addc_u32 s35, s35, 0
	s_add_u32 s4, s4, s23
	s_addc_u32 s5, s5, 0
	s_add_u32 s6, s6, s23
	s_addc_u32 s7, s7, 0
	s_add_u32 s8, s8, s36
	s_addc_u32 s9, s9, 0
	global_load_dwordx4 v[172:175], v231, s[32:33] offset:0
	global_load_dwordx4 v[176:179], v231, s[32:33] offset:1024
	global_load_dwordx4 v[180:183], v231, s[32:33] offset:2048
	global_load_dwordx4 v[184:187], v231, s[32:33] offset:3072
	global_load_dword v235, v232, s[34:35]
	s_add_i32 s23, s18, 1
	s_cmp_lt_i32 s23, s19
	s_cselect_b32 s21, 1, 0
	s_bitcmp0_b32 s18, 0
	s_cselect_b32 s21, s21, 0
	s_lshl_b32 s23, s21, 11
	s_lshl_b32 s36, s21, 6
	v_add_u32_e32 v236, s23, v230
	v_add_u32_e32 v238, s23, v230
	v_add_u32_e32 v237, s36, v232
	global_load_dwordx2 v[2:3], v230, s[4:5] offset:0
	global_load_dwordx2 v[4:5], v230, s[4:5] offset:512
	global_load_dwordx2 v[6:7], v230, s[4:5] offset:1024
	global_load_dwordx2 v[8:9], v230, s[4:5] offset:1536
	global_load_dwordx2 v[10:11], v236, s[4:5] offset:0
	global_load_dwordx2 v[12:13], v236, s[4:5] offset:512
	global_load_dwordx2 v[14:15], v236, s[4:5] offset:1024
	global_load_dwordx2 v[16:17], v236, s[4:5] offset:1536
	s_lshr_b32 s23, s18, 12
	s_cmp_lt_i32 s18, 0x8000
	s_cselect_b32 s20, s23, 8
	s_mul_i32 s0, s20, s22
	s_add_u32 s0, s10, s0
	s_addc_u32 s1, s11, 0
	s_add_u32 s0, s0, 0x3000
	s_addc_u32 s1, s1, 0
	global_load_dwordx4 v[68:71], v231, s[0:1] offset:0
	global_load_dwordx4 v[72:75], v231, s[0:1] offset:1024
	global_load_dwordx4 v[76:79], v231, s[0:1] offset:2048
	global_load_dwordx4 v[80:83], v231, s[0:1] offset:3072
	s_add_u32 s0, s0, 0x1000
	s_addc_u32 s1, s1, 0
	global_load_dwordx4 v[52:55], v231, s[0:1] offset:0
	global_load_dwordx4 v[56:59], v231, s[0:1] offset:1024
	global_load_dwordx4 v[60:63], v231, s[0:1] offset:2048
	global_load_dwordx4 v[64:67], v231, s[0:1] offset:3072
	s_waitcnt vmcnt(28)
	ds_write_b128 v221, v[116:119] offset:0
	s_waitcnt vmcnt(27)
	ds_write_b128 v221, v[120:123] offset:512
	s_waitcnt vmcnt(26)
	ds_write_b128 v221, v[124:127] offset:16384
	s_waitcnt vmcnt(25)
	ds_write_b128 v221, v[128:131] offset:16896
	s_waitcnt vmcnt(24)
	ds_write_b128 v221, v[132:135] offset:32768
	s_waitcnt vmcnt(23)
	ds_write_b128 v221, v[136:139] offset:33280
	s_waitcnt vmcnt(22)
	ds_write_b128 v221, v[140:143] offset:49152
	s_waitcnt vmcnt(21)
	ds_write_b128 v221, v[144:147] offset:49664
	s_waitcnt vmcnt(0) lgkmcnt(0)
	s_barrier
	v_add_f32_e32 v52, 1.0, v52
	v_add_f32_e32 v53, 1.0, v53
	v_add_f32_e32 v54, 1.0, v54
	v_add_f32_e32 v55, 1.0, v55
	v_add_f32_e32 v56, 1.0, v56
	v_add_f32_e32 v57, 1.0, v57
	v_add_f32_e32 v58, 1.0, v58
	v_add_f32_e32 v59, 1.0, v59
	v_add_f32_e32 v60, 1.0, v60
	v_add_f32_e32 v61, 1.0, v61
	v_add_f32_e32 v62, 1.0, v62
	v_add_f32_e32 v63, 1.0, v63
	v_add_f32_e32 v64, 1.0, v64
	v_add_f32_e32 v65, 1.0, v65
	v_add_f32_e32 v66, 1.0, v66
	v_add_f32_e32 v67, 1.0, v67
	v_mul_f32_e32 v52, v172, v52
	v_mul_f32_e32 v53, v173, v53
	v_mul_f32_e32 v54, v174, v54
	v_mul_f32_e32 v55, v175, v55
	v_mul_f32_e32 v56, v176, v56
	v_mul_f32_e32 v57, v177, v57
	v_mul_f32_e32 v58, v178, v58
	v_mul_f32_e32 v59, v179, v59
	v_mul_f32_e32 v60, v180, v60
	v_mul_f32_e32 v61, v181, v61
	v_mul_f32_e32 v62, v182, v62
	v_mul_f32_e32 v63, v183, v63
	v_mul_f32_e32 v64, v184, v64
	v_mul_f32_e32 v65, v185, v65
	v_mul_f32_e32 v66, v186, v66
	v_mul_f32_e32 v67, v187, v67
	s_branch .Ln2_loop
.Ln2_idle:
	s_waitcnt vmcnt(7)
	ds_write_b128 v221, v[116:119] offset:0
	s_waitcnt vmcnt(6)
	ds_write_b128 v221, v[120:123] offset:512
	s_waitcnt vmcnt(5)
	ds_write_b128 v221, v[124:127] offset:16384
	s_waitcnt vmcnt(4)
	ds_write_b128 v221, v[128:131] offset:16896
	s_waitcnt vmcnt(3)
	ds_write_b128 v221, v[132:135] offset:32768
	s_waitcnt vmcnt(2)
	ds_write_b128 v221, v[136:139] offset:33280
	s_waitcnt vmcnt(1)
	ds_write_b128 v221, v[140:143] offset:49152
	s_waitcnt vmcnt(0)
	ds_write_b128 v221, v[144:147] offset:49664
	s_waitcnt lgkmcnt(0)
	s_barrier
	s_branch .Ln2_done
